# router tile loop (hot copies of both layers): third per-tile workgroup barrier removed from the loop, one barrier at the loop exit before the histogram is read
# speedup vs baseline: 1.0001x; 1.0001x over previous
.LBB0_1045:
	s_or_b64 exec, exec, s[14:15]
	s_waitcnt vmcnt(8)
	v_lshlrev_b32_e32 v66, 16, v68
	v_and_b32_e32 v67, 0xffff0000, v68
	v_lshlrev_b32_e32 v68, 16, v69
	v_and_b32_e32 v69, 0xffff0000, v69
	v_lshlrev_b32_e32 v70, 16, v72
	v_and_b32_e32 v71, 0xffff0000, v72
	v_lshlrev_b32_e32 v72, 16, v73
	v_and_b32_e32 v73, 0xffff0000, v73
	v_lshlrev_b32_e32 v74, 16, v76
	v_and_b32_e32 v75, 0xffff0000, v76
	v_lshlrev_b32_e32 v76, 16, v77
	v_and_b32_e32 v77, 0xffff0000, v77
	v_lshlrev_b32_e32 v78, 16, v80
	v_and_b32_e32 v79, 0xffff0000, v80
	v_lshlrev_b32_e32 v80, 16, v81
	v_and_b32_e32 v81, 0xffff0000, v81
	v_lshlrev_b32_e32 v82, 16, v84
	v_and_b32_e32 v83, 0xffff0000, v84
	v_lshlrev_b32_e32 v84, 16, v85
	v_and_b32_e32 v85, 0xffff0000, v85
	v_lshlrev_b32_e32 v86, 16, v88
	v_and_b32_e32 v87, 0xffff0000, v88
	v_lshlrev_b32_e32 v88, 16, v89
	v_and_b32_e32 v89, 0xffff0000, v89
	v_lshlrev_b32_e32 v90, 16, v92
	v_and_b32_e32 v91, 0xffff0000, v92
	v_lshlrev_b32_e32 v92, 16, v93
	v_and_b32_e32 v93, 0xffff0000, v93
	v_lshlrev_b32_e32 v94, 16, v96
	v_and_b32_e32 v95, 0xffff0000, v96
	v_lshlrev_b32_e32 v96, 16, v97
	v_and_b32_e32 v97, 0xffff0000, v97
	v_add_u32_e32 v134, s66, v134
	v_add_u32_e32 v107, s73, v134
	v_cmp_le_i32_e32 vcc, s37, v107
	v_add_u32_e32 v106, s70, v106
	v_add_u32_e32 v143, s71, v143
	s_or_b64 s[50:51], vcc, s[50:51]
	v_add_u32_e32 v144, s71, v144
	s_waitcnt lgkmcnt(0)
	s_andn2_b64 exec, exec, s[50:51]
	s_cbranch_execz .LBB0_1090

.LBB0_1090:
	s_or_b64 exec, exec, s[44:45]
	s_barrier
	s_and_saveexec_b64 s[6:7], s[4:5]
	s_cbranch_execz .LBB0_1092
	s_waitcnt vmcnt(61)
	v_add_u32_e32 v2, 0x14400, v136
	ds_read_b32 v2, v2
	v_ashrrev_i32_e32 v147, 31, v146
	v_lshl_add_u64 v[0:1], v[146:147], 2, s[34:35]
	v_add_co_u32_e32 v0, vcc, 0x1000, v0
	s_nop 1
	v_addc_co_u32_e32 v1, vcc, 0, v1, vcc
	s_waitcnt lgkmcnt(0)
	global_atomic_add v0, v[0:1], v2, off sc0
	v_add_u32_e32 v1, 0x14480, v136
	s_waitcnt vmcnt(0)
	ds_write_b32 v1, v0

.LBB0_3006:
	s_or_b64 exec, exec, s[16:17]
	s_waitcnt vmcnt(8)
	v_lshlrev_b32_e32 v66, 16, v70
	v_and_b32_e32 v67, 0xffff0000, v70
	v_lshlrev_b32_e32 v68, 16, v71
	v_and_b32_e32 v69, 0xffff0000, v71
	v_lshlrev_b32_e32 v70, 16, v72
	v_and_b32_e32 v71, 0xffff0000, v72
	v_lshlrev_b32_e32 v72, 16, v73
	v_and_b32_e32 v73, 0xffff0000, v73
	v_lshlrev_b32_e32 v74, 16, v76
	v_and_b32_e32 v75, 0xffff0000, v76
	v_lshlrev_b32_e32 v76, 16, v77
	v_and_b32_e32 v77, 0xffff0000, v77
	v_lshlrev_b32_e32 v78, 16, v80
	v_and_b32_e32 v79, 0xffff0000, v80
	v_lshlrev_b32_e32 v80, 16, v81
	v_and_b32_e32 v81, 0xffff0000, v81
	v_lshlrev_b32_e32 v82, 16, v84
	v_and_b32_e32 v83, 0xffff0000, v84
	v_lshlrev_b32_e32 v84, 16, v85
	v_and_b32_e32 v85, 0xffff0000, v85
	v_lshlrev_b32_e32 v86, 16, v88
	v_and_b32_e32 v87, 0xffff0000, v88
	v_lshlrev_b32_e32 v88, 16, v89
	v_and_b32_e32 v89, 0xffff0000, v89
	v_lshlrev_b32_e32 v90, 16, v92
	v_and_b32_e32 v91, 0xffff0000, v92
	v_lshlrev_b32_e32 v92, 16, v93
	v_and_b32_e32 v93, 0xffff0000, v93
	v_lshlrev_b32_e32 v94, 16, v96
	v_and_b32_e32 v95, 0xffff0000, v96
	v_lshlrev_b32_e32 v96, 16, v97
	v_and_b32_e32 v97, 0xffff0000, v97
	s_and_b64 s[14:15], exec, s[14:15]
	s_or_b64 s[34:35], s[14:15], s[34:35]
	v_add_u32_e32 v108, s56, v108
	s_add_i32 s53, s53, s57
	s_waitcnt lgkmcnt(0)
	s_andn2_b64 exec, exec, s[34:35]
	s_cbranch_execz .LBB0_3051

.LBB0_3051:
	s_or_b64 exec, exec, s[26:27]
	s_barrier
	s_and_saveexec_b64 s[6:7], s[2:3]
	s_cbranch_execz .LBB0_3053
	s_waitcnt vmcnt(61)
	v_lshl_add_u32 v2, v64, 2, 0
	s_waitcnt vmcnt(60)
	v_add_u32_e32 v3, 0x14400, v2
	ds_read_b32 v3, v3
	v_ashrrev_i32_e32 v65, 31, v64
	v_lshl_add_u64 v[0:1], v[64:65], 2, s[20:21]
	v_add_co_u32_e32 v0, vcc, 0x1000, v0
	s_nop 1
	v_addc_co_u32_e32 v1, vcc, 0, v1, vcc
	s_waitcnt lgkmcnt(0)
	global_atomic_add v0, v[0:1], v3, off offset:128 sc0
	v_add_u32_e32 v1, 0x14480, v2
	s_waitcnt vmcnt(0)
	ds_write_b32 v1, v0
